# phase 12: nt cache hint on the final output stores and on the once-read expert-output gather loads; on top of v45
# speedup vs baseline: 1.0084x; 1.0027x over previous
; #define GAS __attribute__((address_space(1)))
; __device__ __forceinline__ void phase12(KP kp, LAS unsigned char* lds, int wave, int bid, int G) {
;     ...
;         const i32x4 te = *(const GAS i32x4*)(TOPI + m * 4), rk = *(const GAS i32x4*)(TRANK + m * 4); const f32x4 tw = *(const GAS f32x4*)(TOPW + m * 4);
;         const i32x4 sl = (i32x4){pstart[te.x] + rk.x, pstart[te.y] + rk.y, pstart[te.z] + rk.z, pstart[te.w] + rk.w};
;         const GAS u32x2* y0 = (const GAS u32x2*)(YS + (size_t)sl.x * DM) + lane; const GAS u32x2* y1 = (const GAS u32x2*)(YS + (size_t)sl.y * DM) + lane;
;         const GAS u32x2* y2 = (const GAS u32x2*)(YS + (size_t)sl.z * DM) + lane; const GAS u32x2* y3 = (const GAS u32x2*)(YS + (size_t)sl.w * DM) + lane;
.Lp12_nopf:
	s_cmpk_lt_i32 s2, 0x2000
	v_lshlrev_b32_e32 v103, 2, v104
	v_lshlrev_b32_e32 v104, 2, v105
	v_lshlrev_b32_e32 v105, 2, v106
	v_lshlrev_b32_e32 v106, 2, v107
	v_add_u32_e32 v103, s3, v103
	v_add_u32_e32 v105, s3, v105
	v_add_u32_e32 v104, s3, v104
	v_add_u32_e32 v106, s3, v106
	ds_read_b32 v103, v103
	ds_read_b32 v107, v104
	ds_read_b32 v105, v105
	ds_read_b32 v116, v106
	s_waitcnt lgkmcnt(3)
	v_add_u32_e32 v106, v103, v108
	s_waitcnt lgkmcnt(2)
	v_add_u32_e32 v108, v107, v109
	s_waitcnt lgkmcnt(1)
	v_add_u32_e32 v110, v105, v110
	s_waitcnt lgkmcnt(0)
	v_add_u32_e32 v116, v116, v111
	v_ashrrev_i32_e32 v107, 31, v106
	v_ashrrev_i32_e32 v109, 31, v108
	v_ashrrev_i32_e32 v111, 31, v110
	v_ashrrev_i32_e32 v117, 31, v116
	v_lshlrev_b64 v[106:107], 12, v[106:107]
	v_lshlrev_b64 v[108:109], 12, v[108:109]
	v_lshlrev_b64 v[110:111], 12, v[110:111]
	v_lshlrev_b64 v[116:117], 12, v[116:117]
	v_lshl_add_u64 v[106:107], v[68:69], 0, v[106:107]
	v_lshl_add_u64 v[108:109], v[68:69], 0, v[108:109]
	v_lshl_add_u64 v[110:111], v[68:69], 0, v[110:111]
	v_lshl_add_u64 v[116:117], v[68:69], 0, v[116:117]
	global_load_dwordx2 v[118:119], v[106:107], off nt
	global_load_dwordx2 v[120:121], v[108:109], off nt
	global_load_dwordx2 v[122:123], v[110:111], off nt
	global_load_dwordx2 v[124:125], v[116:117], off nt
	global_load_dwordx2 v[126:127], v[106:107], off offset:512 nt
	global_load_dwordx2 v[128:129], v[108:109], off offset:512 nt
	global_load_dwordx2 v[130:131], v[110:111], off offset:512 nt
	global_load_dwordx2 v[132:133], v[116:117], off offset:512 nt
	global_load_dwordx2 v[134:135], v[106:107], off offset:1024 nt
	global_load_dwordx2 v[136:137], v[108:109], off offset:1024 nt
	global_load_dwordx2 v[138:139], v[110:111], off offset:1024 nt
	global_load_dwordx2 v[140:141], v[116:117], off offset:1024 nt
	global_load_dwordx2 v[142:143], v[106:107], off offset:1536 nt
	global_load_dwordx2 v[144:145], v[108:109], off offset:1536 nt
	global_load_dwordx2 v[146:147], v[110:111], off offset:1536 nt
	global_load_dwordx2 v[148:149], v[116:117], off offset:1536 nt
	global_load_dwordx2 v[150:151], v[106:107], off offset:2048 nt
	global_load_dwordx2 v[152:153], v[106:107], off offset:2560 nt
	global_load_dwordx2 v[154:155], v[106:107], off offset:3072 nt
	s_nop 0
	global_load_dwordx2 v[106:107], v[106:107], off offset:3584 nt
	s_nop 0
	global_load_dwordx2 v[156:157], v[108:109], off offset:2048 nt
	global_load_dwordx2 v[158:159], v[108:109], off offset:2560 nt
	global_load_dwordx2 v[160:161], v[108:109], off offset:3072 nt
	s_nop 0
	global_load_dwordx2 v[108:109], v[108:109], off offset:3584 nt
	s_nop 0
	global_load_dwordx2 v[162:163], v[110:111], off offset:2048 nt
	global_load_dwordx2 v[164:165], v[110:111], off offset:2560 nt
	global_load_dwordx2 v[166:167], v[110:111], off offset:3072 nt
	s_nop 0
	global_load_dwordx2 v[110:111], v[110:111], off offset:3584 nt
	s_nop 0
	global_load_dwordx2 v[168:169], v[116:117], off offset:2048 nt
	global_load_dwordx2 v[170:171], v[116:117], off offset:2560 nt
	global_load_dwordx2 v[172:173], v[116:117], off offset:3072 nt
	s_nop 0
	global_load_dwordx2 v[116:117], v[116:117], off offset:3584 nt
	s_waitcnt vmcnt(31)
	v_mov_b32_e32 v104, v115
	v_lshlrev_b32_e32 v174, 16, v118
	s_waitcnt vmcnt(30)
	v_lshlrev_b32_e32 v176, 16, v120
	v_and_b32_e32 v177, 0xffff0000, v120
	v_lshlrev_b32_e32 v120, 16, v121
	v_and_b32_e32 v121, 0xffff0000, v121
	s_waitcnt vmcnt(26)
	v_lshlrev_b32_e32 v184, 16, v128
	v_and_b32_e32 v185, 0xffff0000, v128
	v_lshlrev_b32_e32 v128, 16, v129
	v_and_b32_e32 v129, 0xffff0000, v129
	v_and_b32_e32 v175, 0xffff0000, v118
	v_lshlrev_b32_e32 v118, 16, v119
	v_and_b32_e32 v119, 0xffff0000, v119
	v_lshlrev_b32_e32 v182, 16, v126
	v_and_b32_e32 v183, 0xffff0000, v126
	v_lshlrev_b32_e32 v126, 16, v127
	v_and_b32_e32 v127, 0xffff0000, v127
	s_waitcnt vmcnt(22)
	v_lshlrev_b32_e32 v192, 16, v136
	v_and_b32_e32 v193, 0xffff0000, v136
	v_lshlrev_b32_e32 v136, 16, v137
	v_and_b32_e32 v137, 0xffff0000, v137
	s_waitcnt vmcnt(18)
	v_lshlrev_b32_e32 v200, 16, v144
	v_and_b32_e32 v201, 0xffff0000, v144
	v_lshlrev_b32_e32 v144, 16, v145
	v_and_b32_e32 v145, 0xffff0000, v145
	s_waitcnt vmcnt(11)
	v_lshlrev_b32_e32 v208, 16, v156
	v_and_b32_e32 v209, 0xffff0000, v156
	v_lshlrev_b32_e32 v156, 16, v157
	v_and_b32_e32 v157, 0xffff0000, v157
	s_waitcnt vmcnt(10)
	v_lshlrev_b32_e32 v216, 16, v158
	v_and_b32_e32 v217, 0xffff0000, v158
	v_lshlrev_b32_e32 v158, 16, v159
	v_and_b32_e32 v159, 0xffff0000, v159
	s_waitcnt vmcnt(9)
	v_lshlrev_b32_e32 v224, 16, v160
	v_and_b32_e32 v225, 0xffff0000, v160
	v_lshlrev_b32_e32 v160, 16, v161
	v_and_b32_e32 v161, 0xffff0000, v161
	s_waitcnt vmcnt(8)
; __device__ __forceinline__ f32x4 unpack4(u32x2 w) { return (f32x4){bflo(w.x), bfhi(w.x), bflo(w.y), bfhi(w.y)}; }
; __device__ __forceinline__ void phase12(KP kp, LAS unsigned char* lds, int wave, int bid, int G) {
;     ...
;         for (int j = 0; j < 8; ++j) {
;             const f32x4 mo = tw.x * unpack4(y0[64 * j]) + tw.y * unpack4(y1[64 * j]) + tw.z * unpack4(y2[64 * j]) + tw.w * unpack4(y3[64 * j]);
	v_lshlrev_b32_e32 v232, 16, v108
	v_and_b32_e32 v233, 0xffff0000, v108
	v_lshlrev_b32_e32 v108, 16, v109
	v_and_b32_e32 v109, 0xffff0000, v109
	v_pk_mul_f32 v[120:121], v[112:113], v[120:121] op_sel:[1,0]
	v_pk_mul_f32 v[176:177], v[112:113], v[176:177] op_sel:[1,0]
	v_pk_mul_f32 v[128:129], v[112:113], v[128:129] op_sel:[1,0]
	v_pk_mul_f32 v[184:185], v[112:113], v[184:185] op_sel:[1,0]
	v_lshlrev_b32_e32 v178, 16, v122
	v_and_b32_e32 v179, 0xffff0000, v122
	v_lshlrev_b32_e32 v122, 16, v123
	v_and_b32_e32 v123, 0xffff0000, v123
	v_lshlrev_b32_e32 v186, 16, v130
	v_and_b32_e32 v187, 0xffff0000, v130
	v_lshlrev_b32_e32 v130, 16, v131
	v_and_b32_e32 v131, 0xffff0000, v131
	v_lshlrev_b32_e32 v190, 16, v134
	v_and_b32_e32 v191, 0xffff0000, v134
	v_lshlrev_b32_e32 v134, 16, v135
	v_and_b32_e32 v135, 0xffff0000, v135
	v_lshlrev_b32_e32 v198, 16, v142
	v_and_b32_e32 v199, 0xffff0000, v142
	v_lshlrev_b32_e32 v142, 16, v143
	v_and_b32_e32 v143, 0xffff0000, v143
	v_lshlrev_b32_e32 v206, 16, v150
	v_and_b32_e32 v207, 0xffff0000, v150
	v_lshlrev_b32_e32 v150, 16, v151
	v_and_b32_e32 v151, 0xffff0000, v151
	v_lshlrev_b32_e32 v214, 16, v152
	v_and_b32_e32 v215, 0xffff0000, v152
	v_lshlrev_b32_e32 v152, 16, v153
	v_and_b32_e32 v153, 0xffff0000, v153
	v_lshlrev_b32_e32 v222, 16, v154
	v_and_b32_e32 v223, 0xffff0000, v154
	v_lshlrev_b32_e32 v154, 16, v155
	v_and_b32_e32 v155, 0xffff0000, v155
	v_lshlrev_b32_e32 v230, 16, v106
	v_and_b32_e32 v231, 0xffff0000, v106
	v_lshlrev_b32_e32 v106, 16, v107
	v_and_b32_e32 v107, 0xffff0000, v107
	v_pk_mul_f32 v[192:193], v[112:113], v[192:193] op_sel:[1,0]
	v_pk_mul_f32 v[136:137], v[112:113], v[136:137] op_sel:[1,0]
	v_pk_mul_f32 v[144:145], v[112:113], v[144:145] op_sel:[1,0]
	v_pk_mul_f32 v[200:201], v[112:113], v[200:201] op_sel:[1,0]
	v_pk_mul_f32 v[156:157], v[112:113], v[156:157] op_sel:[1,0]
	v_pk_mul_f32 v[208:209], v[112:113], v[208:209] op_sel:[1,0]
	v_pk_mul_f32 v[216:217], v[112:113], v[216:217] op_sel:[1,0]
	v_pk_mul_f32 v[158:159], v[112:113], v[158:159] op_sel:[1,0]
	v_pk_mul_f32 v[160:161], v[112:113], v[160:161] op_sel:[1,0]
	v_pk_mul_f32 v[224:225], v[112:113], v[224:225] op_sel:[1,0]
	v_pk_mul_f32 v[108:109], v[112:113], v[108:109] op_sel:[1,0]
	v_pk_mul_f32 v[232:233], v[112:113], v[232:233] op_sel:[1,0]
	v_pk_fma_f32 v[174:175], v[112:113], v[174:175], v[176:177] op_sel_hi:[0,1,1]
	v_pk_fma_f32 v[118:119], v[112:113], v[118:119], v[120:121] op_sel_hi:[0,1,1]
	v_pk_fma_f32 v[120:121], v[112:113], v[182:183], v[184:185] op_sel_hi:[0,1,1]
	v_pk_fma_f32 v[126:127], v[112:113], v[126:127], v[128:129] op_sel_hi:[0,1,1]
	v_lshlrev_b32_e32 v180, 16, v124
	v_and_b32_e32 v181, 0xffff0000, v124
	v_lshlrev_b32_e32 v124, 16, v125
	v_and_b32_e32 v125, 0xffff0000, v125
	v_lshlrev_b32_e32 v188, 16, v132
	v_and_b32_e32 v189, 0xffff0000, v132
	v_lshlrev_b32_e32 v132, 16, v133
	v_and_b32_e32 v133, 0xffff0000, v133
	v_lshlrev_b32_e32 v194, 16, v138
	v_and_b32_e32 v195, 0xffff0000, v138
	v_lshlrev_b32_e32 v138, 16, v139
	v_and_b32_e32 v139, 0xffff0000, v139
	v_lshlrev_b32_e32 v202, 16, v146
	v_and_b32_e32 v203, 0xffff0000, v146
	v_lshlrev_b32_e32 v146, 16, v147
	v_and_b32_e32 v147, 0xffff0000, v147
	s_waitcnt vmcnt(7)
	v_lshlrev_b32_e32 v210, 16, v162
	v_and_b32_e32 v211, 0xffff0000, v162
	v_lshlrev_b32_e32 v162, 16, v163
	v_and_b32_e32 v163, 0xffff0000, v163
	s_waitcnt vmcnt(6)
	v_lshlrev_b32_e32 v218, 16, v164
	v_and_b32_e32 v219, 0xffff0000, v164
	v_lshlrev_b32_e32 v164, 16, v165
	v_and_b32_e32 v165, 0xffff0000, v165
	s_waitcnt vmcnt(5)
	v_lshlrev_b32_e32 v226, 16, v166
	v_and_b32_e32 v227, 0xffff0000, v166
	v_lshlrev_b32_e32 v166, 16, v167
	v_and_b32_e32 v167, 0xffff0000, v167
	s_waitcnt vmcnt(4)
	v_lshlrev_b32_e32 v234, 16, v110
	v_and_b32_e32 v235, 0xffff0000, v110
	v_lshlrev_b32_e32 v110, 16, v111
	v_and_b32_e32 v111, 0xffff0000, v111
	v_pk_fma_f32 v[128:129], v[112:113], v[134:135], v[136:137] op_sel_hi:[0,1,1]
	v_pk_fma_f32 v[134:135], v[112:113], v[190:191], v[192:193] op_sel_hi:[0,1,1]
	v_pk_fma_f32 v[136:137], v[112:113], v[198:199], v[200:201] op_sel_hi:[0,1,1]
	v_pk_fma_f32 v[142:143], v[112:113], v[142:143], v[144:145] op_sel_hi:[0,1,1]
	v_pk_fma_f32 v[144:145], v[112:113], v[206:207], v[208:209] op_sel_hi:[0,1,1]
	v_pk_fma_f32 v[150:151], v[112:113], v[150:151], v[156:157] op_sel_hi:[0,1,1]
	v_pk_fma_f32 v[152:153], v[112:113], v[152:153], v[158:159] op_sel_hi:[0,1,1]
	v_pk_fma_f32 v[156:157], v[112:113], v[214:215], v[216:217] op_sel_hi:[0,1,1]
	v_pk_fma_f32 v[158:159], v[112:113], v[222:223], v[224:225] op_sel_hi:[0,1,1]
	v_pk_fma_f32 v[154:155], v[112:113], v[154:155], v[160:161] op_sel_hi:[0,1,1]
	v_pk_fma_f32 v[160:161], v[112:113], v[230:231], v[232:233] op_sel_hi:[0,1,1]
	v_pk_fma_f32 v[106:107], v[112:113], v[106:107], v[108:109] op_sel_hi:[0,1,1]
	v_pk_fma_f32 v[108:109], v[114:115], v[122:123], v[118:119] op_sel_hi:[0,1,1]
	v_pk_fma_f32 v[112:113], v[114:115], v[178:179], v[174:175] op_sel_hi:[0,1,1]
	v_pk_fma_f32 v[118:119], v[114:115], v[130:131], v[126:127] op_sel_hi:[0,1,1]
	v_pk_fma_f32 v[120:121], v[114:115], v[186:187], v[120:121] op_sel_hi:[0,1,1]
	v_lshlrev_b32_e32 v196, 16, v140
	v_and_b32_e32 v197, 0xffff0000, v140
	v_lshlrev_b32_e32 v140, 16, v141
	v_and_b32_e32 v141, 0xffff0000, v141
	v_lshlrev_b32_e32 v204, 16, v148
	v_and_b32_e32 v205, 0xffff0000, v148
	v_lshlrev_b32_e32 v148, 16, v149
	v_and_b32_e32 v149, 0xffff0000, v149
	s_waitcnt vmcnt(3)
	v_lshlrev_b32_e32 v212, 16, v168
	v_and_b32_e32 v213, 0xffff0000, v168
	v_lshlrev_b32_e32 v168, 16, v169
	v_and_b32_e32 v169, 0xffff0000, v169
	s_waitcnt vmcnt(2)
; #define GAS __attribute__((address_space(1)))
; __device__ __forceinline__ float dot4(f32x4 a, f32x4 b) { return (a.x * b.x + a.y * b.y) + (a.z * b.z + a.w * b.w); }
; __device__ __forceinline__ f32x4 unpack4(u32x2 w) { return (f32x4){bflo(w.x), bfhi(w.x), bflo(w.y), bfhi(w.y)}; }
; __device__ __forceinline__ void phase12(KP kp, LAS unsigned char* lds, int wave, int bid, int G) {
;     ...
;             const f32x4 mo = tw.x * unpack4(y0[64 * j]) + tw.y * unpack4(y1[64 * j]) + tw.z * unpack4(y2[64 * j]) + tw.w * unpack4(y3[64 * j]);
;             const f32x4 g2 = *(const GAS f32x4*)(mod + 5 * 2048 + 256 * j + 4 * lane);
;             v[j] = xr[64 * j] + g2 * mo; s += dot4(v[j], v[j]); }
	v_lshlrev_b32_e32 v220, 16, v170
	v_and_b32_e32 v221, 0xffff0000, v170
	v_lshlrev_b32_e32 v170, 16, v171
	v_and_b32_e32 v171, 0xffff0000, v171
	s_waitcnt vmcnt(1)
	v_lshlrev_b32_e32 v228, 16, v172
	v_and_b32_e32 v229, 0xffff0000, v172
	v_lshlrev_b32_e32 v172, 16, v173
	v_and_b32_e32 v173, 0xffff0000, v173
	s_waitcnt vmcnt(0)
	v_lshlrev_b32_e32 v236, 16, v116
	v_and_b32_e32 v237, 0xffff0000, v116
	v_lshlrev_b32_e32 v116, 16, v117
	v_and_b32_e32 v117, 0xffff0000, v117
	v_pk_fma_f32 v[122:123], v[114:115], v[194:195], v[134:135] op_sel_hi:[0,1,1]
	v_pk_fma_f32 v[126:127], v[114:115], v[138:139], v[128:129] op_sel_hi:[0,1,1]
	v_pk_fma_f32 v[128:129], v[114:115], v[146:147], v[142:143] op_sel_hi:[0,1,1]
	v_pk_fma_f32 v[130:131], v[114:115], v[202:203], v[136:137] op_sel_hi:[0,1,1]
	v_pk_fma_f32 v[134:135], v[114:115], v[162:163], v[150:151] op_sel_hi:[0,1,1]
	v_pk_fma_f32 v[136:137], v[114:115], v[210:211], v[144:145] op_sel_hi:[0,1,1]
	v_pk_fma_f32 v[138:139], v[114:115], v[218:219], v[156:157] op_sel_hi:[0,1,1]
	v_pk_fma_f32 v[142:143], v[114:115], v[164:165], v[152:153] op_sel_hi:[0,1,1]
	v_pk_fma_f32 v[144:145], v[114:115], v[166:167], v[154:155] op_sel_hi:[0,1,1]
	v_pk_fma_f32 v[146:147], v[114:115], v[226:227], v[158:159] op_sel_hi:[0,1,1]
	v_pk_fma_f32 v[106:107], v[114:115], v[110:111], v[106:107] op_sel_hi:[0,1,1]
	v_pk_fma_f32 v[110:111], v[114:115], v[234:235], v[160:161] op_sel_hi:[0,1,1]
	v_pk_fma_f32 v[112:113], v[104:105], v[180:181], v[112:113] op_sel_hi:[0,1,1]
	v_pk_fma_f32 v[108:109], v[104:105], v[124:125], v[108:109] op_sel_hi:[0,1,1]
	v_pk_fma_f32 v[114:115], v[104:105], v[188:189], v[120:121] op_sel_hi:[0,1,1]
	v_pk_fma_f32 v[118:119], v[104:105], v[132:133], v[118:119] op_sel_hi:[0,1,1]
	v_pk_fma_f32 v[120:121], v[104:105], v[140:141], v[126:127] op_sel_hi:[0,1,1]
	v_pk_fma_f32 v[122:123], v[104:105], v[196:197], v[122:123] op_sel_hi:[0,1,1]
	v_pk_fma_f32 v[124:125], v[104:105], v[204:205], v[130:131] op_sel_hi:[0,1,1]
	v_pk_fma_f32 v[126:127], v[104:105], v[148:149], v[128:129] op_sel_hi:[0,1,1]
	v_pk_fma_f32 v[128:129], v[104:105], v[212:213], v[136:137] op_sel_hi:[0,1,1]
	v_pk_fma_f32 v[130:131], v[104:105], v[168:169], v[134:135] op_sel_hi:[0,1,1]
	v_pk_fma_f32 v[132:133], v[104:105], v[170:171], v[142:143] op_sel_hi:[0,1,1]
	v_pk_fma_f32 v[134:135], v[104:105], v[220:221], v[138:139] op_sel_hi:[0,1,1]
	v_pk_fma_f32 v[136:137], v[104:105], v[228:229], v[146:147] op_sel_hi:[0,1,1]
	v_pk_fma_f32 v[138:139], v[104:105], v[172:173], v[144:145] op_sel_hi:[0,1,1]
	v_pk_fma_f32 v[110:111], v[104:105], v[236:237], v[110:111] op_sel_hi:[0,1,1]
	v_pk_fma_f32 v[104:105], v[104:105], v[116:117], v[106:107] op_sel_hi:[0,1,1]
	v_pk_fma_f32 v[2:3], v[2:3], v[108:109], v[66:67]
	v_pk_fma_f32 v[0:1], v[0:1], v[112:113], v[64:65]
	v_pk_fma_f32 v[6:7], v[6:7], v[118:119], v[62:63]
	v_pk_fma_f32 v[4:5], v[4:5], v[114:115], v[60:61]
	v_pk_fma_f32 v[8:9], v[8:9], v[122:123], v[56:57]
	v_pk_fma_f32 v[10:11], v[10:11], v[120:121], v[58:59]
	v_pk_fma_f32 v[26:27], v[26:27], v[138:139], v[42:43]
	v_pk_fma_f32 v[34:35], v[34:35], v[104:105], v[38:39]
	v_mov_b32_e32 v38, v1
	v_mov_b32_e32 v39, v5
	v_mov_b32_e32 v42, v3
	v_mov_b32_e32 v43, v7
	v_pk_fma_f32 v[20:21], v[20:21], v[134:135], v[44:45]
	v_pk_fma_f32 v[22:23], v[22:23], v[132:133], v[46:47]
	v_pk_fma_f32 v[24:25], v[24:25], v[136:137], v[40:41]
	v_pk_fma_f32 v[32:33], v[32:33], v[110:111], v[36:37]
	v_mov_b32_e32 v36, v0
	v_mov_b32_e32 v37, v4
	v_mov_b32_e32 v40, v2
	v_mov_b32_e32 v41, v6
	v_pk_mul_f32 v[44:45], v[10:11], v[10:11]
	v_pk_mul_f32 v[46:47], v[8:9], v[8:9]
	v_pk_mul_f32 v[38:39], v[38:39], v[38:39]
	v_pk_mul_f32 v[42:43], v[42:43], v[42:43]
	v_pk_fma_f32 v[14:15], v[14:15], v[126:127], v[50:51]
	v_pk_fma_f32 v[12:13], v[12:13], v[124:125], v[48:49]
	v_pk_mov_b32 v[60:61], v[46:47], v[44:45] op_sel:[1,0]
	v_mov_b32_e32 v47, v45
	v_pk_fma_f32 v[36:37], v[36:37], v[36:37], v[38:39]
	v_pk_fma_f32 v[38:39], v[40:41], v[40:41], v[42:43]
	v_pk_fma_f32 v[18:19], v[18:19], v[130:131], v[54:55]
	v_pk_fma_f32 v[16:17], v[16:17], v[128:129], v[52:53]
	v_mul_f32_e32 v48, v13, v13
	v_mul_f32_e32 v50, v15, v15
	v_pk_add_f32 v[40:41], v[60:61], v[46:47]
	v_pk_add_f32 v[36:37], v[36:37], v[38:39]
	v_mul_f32_e32 v59, v16, v16
	v_mul_f32_e32 v62, v17, v17
	v_mul_f32_e32 v63, v18, v18
	v_mul_f32_e32 v64, v19, v19
	v_pk_fma_f32 v[44:45], v[12:13], v[12:13], v[48:49] op_sel_hi:[1,1,0]
	v_pk_fma_f32 v[48:49], v[14:15], v[14:15], v[50:51] op_sel_hi:[1,1,0]
	v_pk_add_f32 v[38:39], v[40:41], v[40:41] op_sel:[0,1] op_sel_hi:[1,0]
	v_pk_add_f32 v[36:37], v[36:37], v[36:37] op_sel:[0,1] op_sel_hi:[1,0]
	v_pk_mul_f32 v[52:53], v[22:23], v[22:23]
	v_pk_mul_f32 v[54:55], v[20:21], v[20:21]
	v_mov_b32_e32 v45, v63
	v_mov_b32_e32 v49, v64
	v_mov_b32_e32 v39, v62
	v_mov_b32_e32 v37, v59
	v_pk_mov_b32 v[50:51], v[54:55], v[52:53] op_sel:[1,0]
	v_mov_b32_e32 v55, v53
	v_pk_add_f32 v[40:41], v[44:45], v[48:49]
; #define GAS __attribute__((address_space(1)))
; __device__ __forceinline__ void phase12(KP kp, LAS unsigned char* lds, int wave, int bid, int G) {
;     ...
;         const float rstd = 1.0f / sqrtf(wave_sum(s) * (1.0f / DM) + EPS);
;         GAS f32x4* o = (GAS f32x4*)(KOUT() + (size_t)m * DM) + lane;
; #pragma unroll
;         for (int j = 0; j < 8; ++j) o[64 * j] = v[j] * rstd * *(const GAS f32x4*)(fg + 256 * j + 4 * lane);
	v_pk_add_f32 v[36:37], v[36:37], v[38:39]
	v_mul_f32_e32 v56, v25, v25
	v_mul_f32_e32 v58, v27, v27
	v_pk_add_f32 v[42:43], v[50:51], v[54:55]
	v_pk_add_f32 v[36:37], v[36:37], v[40:41]
	v_mul_f32_e32 v65, v32, v32
	v_mul_f32_e32 v66, v33, v33
	v_mul_f32_e32 v67, v34, v34
	v_mul_f32_e32 v103, v35, v35
	v_pk_fma_f32 v[52:53], v[24:25], v[24:25], v[56:57] op_sel_hi:[1,1,0]
	v_pk_fma_f32 v[56:57], v[26:27], v[26:27], v[58:59] op_sel_hi:[1,1,0]
	v_pk_add_f32 v[42:43], v[42:43], v[42:43] op_sel:[0,1] op_sel_hi:[1,0]
	v_pk_add_f32 v[36:37], v[36:37], v[36:37] op_sel:[0,1] op_sel_hi:[1,0]
	v_mov_b32_e32 v53, v67
	v_mov_b32_e32 v57, v103
	v_mov_b32_e32 v43, v66
	v_mov_b32_e32 v37, v65
	v_pk_add_f32 v[44:45], v[52:53], v[56:57]
	v_pk_add_f32 v[36:37], v[36:37], v[42:43]
	s_nop 0
	v_pk_add_f32 v[36:37], v[36:37], v[44:45]
	s_nop 0
	v_add_f32_e32 v36, v36, v37
	s_nop 1
	v_add_f32_dpp v36, v36, v36 quad_perm:[1,0,3,2] row_mask:0xf bank_mask:0xf
	s_nop 1
	v_add_f32_dpp v36, v36, v36 quad_perm:[2,3,0,1] row_mask:0xf bank_mask:0xf
	s_nop 1
	v_add_f32_dpp v36, v36, v36 row_half_mirror row_mask:0xf bank_mask:0xf
	s_nop 1
	v_add_f32_dpp v36, v36, v36 row_mirror row_mask:0xf bank_mask:0xf
	v_mov_b32_e32 v37, v36
	s_nop 1
	v_permlane16_swap_b32_e32 v36, v37
	v_add_f32_e32 v36, v36, v37
	v_mov_b32_e32 v37, v36
	s_nop 1
	v_permlane32_swap_b32_e32 v36, v37
	v_add_f32_e32 v36, v36, v37
	global_load_dwordx4 v[44:47], v[72:73], off offset:1024
	global_load_dwordx4 v[48:51], v[72:73], off offset:2048
	global_load_dwordx4 v[52:55], v[72:73], off offset:3072
	global_load_dwordx4 v[56:59], v[82:83], off
	global_load_dwordx4 v[60:63], v[84:85], off
	global_load_dwordx4 v[64:67], v[86:87], off
	global_load_dwordx4 v[94:97], v[88:89], off
	v_fmamk_f32 v36, v36, 0x3a000000, v101
	v_mul_f32_e32 v37, 0x4f800000, v36
	v_cmp_gt_f32_e32 vcc, s22, v36
	s_nop 1
	v_cndmask_b32_e32 v36, v36, v37, vcc
	v_sqrt_f32_e32 v37, v36
	s_nop 0
	v_add_u32_e32 v38, -1, v37
	v_add_u32_e32 v39, 1, v37
	v_fma_f32 v40, -v38, v37, v36
	v_fma_f32 v41, -v39, v37, v36
	v_cmp_ge_f32_e64 s[0:1], 0, v40
	s_nop 1
	v_cndmask_b32_e64 v37, v37, v38, s[0:1]
	v_cmp_lt_f32_e64 s[0:1], 0, v41
	s_nop 1
	v_cndmask_b32_e64 v37, v37, v39, s[0:1]
	v_mul_f32_e32 v38, 0x37800000, v37
	v_cndmask_b32_e32 v37, v37, v38, vcc
	v_cmp_class_f32_e32 vcc, v36, v102
	s_nop 1
	v_cndmask_b32_e32 v36, v37, v36, vcc
	v_div_scale_f32 v37, s[0:1], v36, v36, 1.0
	v_rcp_f32_e32 v39, v37
	v_div_scale_f32 v38, vcc, 1.0, v36, 1.0
	v_fma_f32 v40, -v37, v39, 1.0
	v_fmac_f32_e32 v39, v40, v39
	v_mul_f32_e32 v40, v38, v39
	v_fma_f32 v41, -v37, v40, v38
	v_fmac_f32_e32 v40, v41, v39
	v_fma_f32 v37, -v37, v40, v38
	v_div_fmas_f32 v37, v37, v39, v40
	v_div_fixup_f32 v36, v37, v36, 1.0
	v_add_co_u32_e32 v38, vcc, s23, v92
	s_nop 1
	v_addc_co_u32_e32 v39, vcc, 0, v93, vcc
	s_waitcnt vmcnt(0)
	v_pk_mul_f32 v[0:1], v[0:1], v[36:37] op_sel_hi:[1,0]
	v_pk_mul_f32 v[2:3], v[2:3], v[36:37] op_sel_hi:[1,0]
	v_pk_mul_f32 v[0:1], v[28:29], v[0:1]
	v_pk_mul_f32 v[2:3], v[30:31], v[2:3]
	global_store_dwordx4 v[92:93], v[0:3], off nt
	v_pk_mul_f32 v[4:5], v[4:5], v[36:37] op_sel_hi:[1,0]
	v_pk_mul_f32 v[6:7], v[6:7], v[36:37] op_sel_hi:[1,0]
	v_pk_mul_f32 v[4:5], v[44:45], v[4:5]
	v_pk_mul_f32 v[6:7], v[46:47], v[6:7]
	global_store_dwordx4 v[92:93], v[4:7], off offset:1024 nt
	v_pk_mul_f32 v[8:9], v[8:9], v[36:37] op_sel_hi:[1,0]
	v_pk_mul_f32 v[10:11], v[10:11], v[36:37] op_sel_hi:[1,0]
	v_pk_mul_f32 v[8:9], v[48:49], v[8:9]
	v_pk_mul_f32 v[10:11], v[50:51], v[10:11]
	global_store_dwordx4 v[92:93], v[8:11], off offset:2048 nt
	v_pk_mul_f32 v[12:13], v[12:13], v[36:37] op_sel_hi:[1,0]
	v_pk_mul_f32 v[14:15], v[14:15], v[36:37] op_sel_hi:[1,0]
	v_pk_mul_f32 v[12:13], v[52:53], v[12:13]
	v_pk_mul_f32 v[14:15], v[54:55], v[14:15]
	global_store_dwordx4 v[92:93], v[12:15], off offset:3072 nt
	v_pk_mul_f32 v[16:17], v[16:17], v[36:37] op_sel_hi:[1,0]
	v_pk_mul_f32 v[18:19], v[18:19], v[36:37] op_sel_hi:[1,0]
	v_pk_mul_f32 v[16:17], v[56:57], v[16:17]
	v_pk_mul_f32 v[18:19], v[58:59], v[18:19]
	global_store_dwordx4 v[38:39], v[16:19], off nt
	v_pk_mul_f32 v[20:21], v[20:21], v[36:37] op_sel_hi:[1,0]
	v_pk_mul_f32 v[22:23], v[22:23], v[36:37] op_sel_hi:[1,0]
	v_pk_mul_f32 v[20:21], v[60:61], v[20:21]
	v_pk_mul_f32 v[22:23], v[62:63], v[22:23]
	global_store_dwordx4 v[38:39], v[20:23], off offset:1024 nt
	v_pk_mul_f32 v[24:25], v[24:25], v[36:37] op_sel_hi:[1,0]
	v_pk_mul_f32 v[26:27], v[26:27], v[36:37] op_sel_hi:[1,0]
	v_pk_mul_f32 v[24:25], v[64:65], v[24:25]
	v_pk_mul_f32 v[26:27], v[66:67], v[26:27]
	global_store_dwordx4 v[38:39], v[24:27], off offset:2048 nt
	v_pk_mul_f32 v[32:33], v[32:33], v[36:37] op_sel_hi:[1,0]
	v_pk_mul_f32 v[34:35], v[34:35], v[36:37] op_sel_hi:[1,0]
	v_pk_mul_f32 v[32:33], v[94:95], v[32:33]
	v_pk_mul_f32 v[34:35], v[96:97], v[34:35]
	global_store_dwordx4 v[38:39], v[32:35], off offset:3072 nt
	s_cbranch_scc1 .LBB0_4682
